# v41 + slot phase: 32 independent histogram loads per thread instead of 16 serialized load-pair iterations
# baseline (speedup 1.0000x reference)
; __device__ __forceinline__ void p11_slots(Frame& F) {
;     ...
;     { const int e = tid & 63, part = tid >> 6; int sa = 0, sp = 0;
;       for (int bb = part * 32; bb < part * 32 + 32; ++bb) { const int c = WSP(int, WS_CNT)[bb * 64 + e]; sa += c; if (bb < b) sp += c; }
;       tot[part * 64 + e] = sa; pre[part * 64 + e] = sp; }
.LBB0_1466:
	s_cmp_lt_i32 s28, 13
	s_cselect_b64 s[6:7], -1, 0
	s_and_b64 s[6:7], s[6:7], s[4:5]
	s_andn2_b64 vcc, exec, s[6:7]
	s_cbranch_vccnz .LBB0_1497
	s_waitcnt vmcnt(0)
	v_mov_b32_e32 v6, v0
	s_mov_b64 s[4:5], s[0:1]
	s_load_dwordx2 s[8:9], s[4:5], 0xc8
	v_ashrrev_i32_e32 v5, 1, v6
	v_and_b32_e32 v2, 0xffffffe0, v5
	v_or_b32_e32 v7, 31, v5
	v_max_i32_e32 v10, v7, v2
	v_add_u32_e32 v1, 1, v10
	s_waitcnt lgkmcnt(0)
	s_add_u32 s10, s8, 0x150000
	v_sub_u32_e32 v9, v1, v2
	v_and_b32_e32 v4, 63, v6
	s_addc_u32 s11, s9, 0
	v_lshl_or_b32 v1, v2, 6, v4
	v_lshlrev_b32_e32 v1, 2, v1
	v_add_u32_e32 v5, 0x1000, v1
	global_load_dword v16, v1, s[10:11]
	global_load_dword v17, v1, s[10:11] offset:256
	global_load_dword v18, v1, s[10:11] offset:512
	global_load_dword v19, v1, s[10:11] offset:768
	global_load_dword v20, v1, s[10:11] offset:1024
	global_load_dword v21, v1, s[10:11] offset:1280
	global_load_dword v22, v1, s[10:11] offset:1536
	global_load_dword v23, v1, s[10:11] offset:1792
	global_load_dword v24, v1, s[10:11] offset:2048
	global_load_dword v25, v1, s[10:11] offset:2304
	global_load_dword v26, v1, s[10:11] offset:2560
	global_load_dword v27, v1, s[10:11] offset:2816
	global_load_dword v28, v1, s[10:11] offset:3072
	global_load_dword v29, v1, s[10:11] offset:3328
	global_load_dword v30, v1, s[10:11] offset:3584
	global_load_dword v31, v1, s[10:11] offset:3840
	global_load_dword v32, v5, s[10:11]
	global_load_dword v33, v5, s[10:11] offset:256
	global_load_dword v34, v5, s[10:11] offset:512
	global_load_dword v35, v5, s[10:11] offset:768
	global_load_dword v36, v5, s[10:11] offset:1024
	global_load_dword v37, v5, s[10:11] offset:1280
	global_load_dword v38, v5, s[10:11] offset:1536
	global_load_dword v39, v5, s[10:11] offset:1792
	global_load_dword v40, v5, s[10:11] offset:2048
	global_load_dword v41, v5, s[10:11] offset:2304
	global_load_dword v42, v5, s[10:11] offset:2560
	global_load_dword v43, v5, s[10:11] offset:2816
	global_load_dword v44, v5, s[10:11] offset:3072
	global_load_dword v45, v5, s[10:11] offset:3328
	global_load_dword v46, v5, s[10:11] offset:3584
	global_load_dword v47, v5, s[10:11] offset:3840
	v_sub_u32_e32 v9, s2, v2
	v_mov_b32_e32 v8, 0
	v_mov_b32_e32 v3, 0
	s_waitcnt vmcnt(0)
	v_cmp_lt_i32_e32 vcc, 0, v9
	v_add_u32_e32 v8, v16, v8
	s_nop 0
	v_cndmask_b32_e32 v7, 0, v16, vcc
	v_add_u32_e32 v3, v7, v3
	v_cmp_lt_i32_e32 vcc, 1, v9
	v_add_u32_e32 v8, v17, v8
	s_nop 0
	v_cndmask_b32_e32 v7, 0, v17, vcc
	v_add_u32_e32 v3, v7, v3
	v_cmp_lt_i32_e32 vcc, 2, v9
	v_add_u32_e32 v8, v18, v8
	s_nop 0
	v_cndmask_b32_e32 v7, 0, v18, vcc
	v_add_u32_e32 v3, v7, v3
	v_cmp_lt_i32_e32 vcc, 3, v9
	v_add_u32_e32 v8, v19, v8
	s_nop 0
	v_cndmask_b32_e32 v7, 0, v19, vcc
	v_add_u32_e32 v3, v7, v3
	v_cmp_lt_i32_e32 vcc, 4, v9
	v_add_u32_e32 v8, v20, v8
	s_nop 0
	v_cndmask_b32_e32 v7, 0, v20, vcc
	v_add_u32_e32 v3, v7, v3
	v_cmp_lt_i32_e32 vcc, 5, v9
	v_add_u32_e32 v8, v21, v8
	s_nop 0
	v_cndmask_b32_e32 v7, 0, v21, vcc
	v_add_u32_e32 v3, v7, v3
	v_cmp_lt_i32_e32 vcc, 6, v9
	v_add_u32_e32 v8, v22, v8
	s_nop 0
	v_cndmask_b32_e32 v7, 0, v22, vcc
	v_add_u32_e32 v3, v7, v3
	v_cmp_lt_i32_e32 vcc, 7, v9
	v_add_u32_e32 v8, v23, v8
	s_nop 0
	v_cndmask_b32_e32 v7, 0, v23, vcc
	v_add_u32_e32 v3, v7, v3
	v_cmp_lt_i32_e32 vcc, 8, v9
	v_add_u32_e32 v8, v24, v8
	s_nop 0
	v_cndmask_b32_e32 v7, 0, v24, vcc
	v_add_u32_e32 v3, v7, v3
	v_cmp_lt_i32_e32 vcc, 9, v9
	v_add_u32_e32 v8, v25, v8
	s_nop 0
	v_cndmask_b32_e32 v7, 0, v25, vcc
	v_add_u32_e32 v3, v7, v3
	v_cmp_lt_i32_e32 vcc, 10, v9
	v_add_u32_e32 v8, v26, v8
	s_nop 0
	v_cndmask_b32_e32 v7, 0, v26, vcc
	v_add_u32_e32 v3, v7, v3
	v_cmp_lt_i32_e32 vcc, 11, v9
	v_add_u32_e32 v8, v27, v8
	s_nop 0
	v_cndmask_b32_e32 v7, 0, v27, vcc
	v_add_u32_e32 v3, v7, v3
	v_cmp_lt_i32_e32 vcc, 12, v9
	v_add_u32_e32 v8, v28, v8
	s_nop 0
	v_cndmask_b32_e32 v7, 0, v28, vcc
	v_add_u32_e32 v3, v7, v3
	v_cmp_lt_i32_e32 vcc, 13, v9
	v_add_u32_e32 v8, v29, v8
	s_nop 0
	v_cndmask_b32_e32 v7, 0, v29, vcc
	v_add_u32_e32 v3, v7, v3
	v_cmp_lt_i32_e32 vcc, 14, v9
	v_add_u32_e32 v8, v30, v8
	s_nop 0
	v_cndmask_b32_e32 v7, 0, v30, vcc
	v_add_u32_e32 v3, v7, v3
	v_cmp_lt_i32_e32 vcc, 15, v9
	v_add_u32_e32 v8, v31, v8
	s_nop 0
	v_cndmask_b32_e32 v7, 0, v31, vcc
	v_add_u32_e32 v3, v7, v3
	v_cmp_lt_i32_e32 vcc, 16, v9
	v_add_u32_e32 v8, v32, v8
	s_nop 0
	v_cndmask_b32_e32 v7, 0, v32, vcc
	v_add_u32_e32 v3, v7, v3
	v_cmp_lt_i32_e32 vcc, 17, v9
	v_add_u32_e32 v8, v33, v8
	s_nop 0
	v_cndmask_b32_e32 v7, 0, v33, vcc
	v_add_u32_e32 v3, v7, v3
	v_cmp_lt_i32_e32 vcc, 18, v9
	v_add_u32_e32 v8, v34, v8
	s_nop 0
	v_cndmask_b32_e32 v7, 0, v34, vcc
	v_add_u32_e32 v3, v7, v3
	v_cmp_lt_i32_e32 vcc, 19, v9
	v_add_u32_e32 v8, v35, v8
	s_nop 0
	v_cndmask_b32_e32 v7, 0, v35, vcc
	v_add_u32_e32 v3, v7, v3
	v_cmp_lt_i32_e32 vcc, 20, v9
	v_add_u32_e32 v8, v36, v8
	s_nop 0
	v_cndmask_b32_e32 v7, 0, v36, vcc
	v_add_u32_e32 v3, v7, v3
	v_cmp_lt_i32_e32 vcc, 21, v9
	v_add_u32_e32 v8, v37, v8
	s_nop 0
	v_cndmask_b32_e32 v7, 0, v37, vcc
	v_add_u32_e32 v3, v7, v3
	v_cmp_lt_i32_e32 vcc, 22, v9
	v_add_u32_e32 v8, v38, v8
	s_nop 0
	v_cndmask_b32_e32 v7, 0, v38, vcc
	v_add_u32_e32 v3, v7, v3
	v_cmp_lt_i32_e32 vcc, 23, v9
	v_add_u32_e32 v8, v39, v8
	s_nop 0
	v_cndmask_b32_e32 v7, 0, v39, vcc
	v_add_u32_e32 v3, v7, v3
	v_cmp_lt_i32_e32 vcc, 24, v9
	v_add_u32_e32 v8, v40, v8
	s_nop 0
	v_cndmask_b32_e32 v7, 0, v40, vcc
	v_add_u32_e32 v3, v7, v3
	v_cmp_lt_i32_e32 vcc, 25, v9
	v_add_u32_e32 v8, v41, v8
	s_nop 0
	v_cndmask_b32_e32 v7, 0, v41, vcc
	v_add_u32_e32 v3, v7, v3
	v_cmp_lt_i32_e32 vcc, 26, v9
	v_add_u32_e32 v8, v42, v8
	s_nop 0
	v_cndmask_b32_e32 v7, 0, v42, vcc
	v_add_u32_e32 v3, v7, v3
	v_cmp_lt_i32_e32 vcc, 27, v9
	v_add_u32_e32 v8, v43, v8
	s_nop 0
	v_cndmask_b32_e32 v7, 0, v43, vcc
	v_add_u32_e32 v3, v7, v3
	v_cmp_lt_i32_e32 vcc, 28, v9
	v_add_u32_e32 v8, v44, v8
	s_nop 0
	v_cndmask_b32_e32 v7, 0, v44, vcc
	v_add_u32_e32 v3, v7, v3
	v_cmp_lt_i32_e32 vcc, 29, v9
	v_add_u32_e32 v8, v45, v8
	s_nop 0
	v_cndmask_b32_e32 v7, 0, v45, vcc
	v_add_u32_e32 v3, v7, v3
	v_cmp_lt_i32_e32 vcc, 30, v9
	v_add_u32_e32 v8, v46, v8
	s_nop 0
	v_cndmask_b32_e32 v7, 0, v46, vcc
	v_add_u32_e32 v3, v7, v3
	v_cmp_lt_i32_e32 vcc, 31, v9
	v_add_u32_e32 v8, v47, v8
	s_nop 0
	v_cndmask_b32_e32 v7, 0, v47, vcc
	v_add_u32_e32 v3, v7, v3
	s_mov_b64 s[4:5], exec
